# router phase: static s_setprio 1 for the four router waves (converter waves stay at 0); on top of v6
# baseline (speedup 1.0000x reference)
.LBB0_1171:
	s_mov_b64 s[4:5], s[86:87]
	s_mov_b32 s8, 0
	s_cmp_lt_i32 s82, 10
	s_cselect_b64 s[6:7], -1, 0
	v_mbcnt_lo_u32_b32 v0, -1, s8
	v_mbcnt_hi_u32_b32 v0, -1, v0
	v_or_b32_e32 v162, s92, v0
	s_and_b64 s[14:15], s[6:7], s[0:1]
	s_andn2_b64 vcc, exec, s[14:15]
	v_readfirstlane_b32 s12, v162
	s_cbranch_vccnz .LBB0_1245
	s_load_dwordx2 s[18:19], s[4:5], 0x138
	s_ashr_i32 s33, s12, 6
	v_and_b32_e32 v65, 63, v162
	s_mov_b64 s[16:17], s[86:87]
	s_cmp_lt_i32 s33, 4
	s_mov_b64 s[0:1], -1
	s_cbranch_scc0 .LBB0_1223
	s_mul_i32 s0, s33, s3
	s_add_i32 s20, s0, s2
	s_cmpk_gt_i32 s20, 0x3ff
	s_cbranch_scc1 .LBB0_1222
	s_setprio 1
	s_waitcnt lgkmcnt(0)
	s_add_u32 s42, s18, 0x900000
	s_mul_i32 s0, s33, 0x5000
	s_addc_u32 s43, s19, 0
	s_add_i32 s13, s0, 0
	s_add_u32 s0, s18, 0x68700000
	v_mov_b32_e32 v67, 0
	v_lshrrev_b32_e32 v8, 4, v65
	s_addc_u32 s1, s19, 0
	v_lshlrev_b32_e32 v0, 3, v65
	v_mov_b32_e32 v1, v67
	v_and_b32_e32 v64, 15, v162
	v_lshl_add_u64 v[68:69], s[0:1], 0, v[0:1]
	v_lshlrev_b32_e32 v0, 10, v8
	v_lshl_add_u64 v[70:71], s[0:1], 0, v[0:1]
	v_lshl_or_b32 v0, v8, 5, v64
	v_mul_u32_u24_e32 v9, 0x110, v0
	v_mov_b32_e32 v0, s13
	s_movk_i32 s0, 0x84
	v_mad_u32_u24 v164, v65, s0, v0
	s_add_i32 s44, 0, 0x18800
	s_add_i32 s0, 0, 0x18880
	s_cmpk_lg_i32 s3, 0x100
	s_cselect_b64 s[26:27], -1, 0
	s_add_u32 s28, s18, 0x10000
	s_addc_u32 s29, s19, 0
	v_lshlrev_b32_e32 v66, 2, v65
	s_cmp_lt_u32 s12, 64
	v_cmp_gt_u32_e32 vcc, 32, v65
	v_add_u32_e32 v168, s0, v66
	s_cselect_b64 s[0:1], -1, 0
	s_and_b64 s[30:31], s[0:1], vcc
	v_or_b32_e32 v6, 0x400, v66
	v_mov_b32_e32 v7, v67
	s_add_u32 s34, s18, 0xb40000
	v_lshlrev_b64 v[78:79], 2, v[6:7]
	v_or_b32_e32 v6, 0x500, v66
	s_addc_u32 s35, s19, 0
	v_lshlrev_b64 v[84:85], 2, v[6:7]
	v_or_b32_e32 v6, 0x600, v66
	s_add_u32 s36, s18, 0xb80000
	s_load_dwordx4 s[8:11], s[16:17], 0xd0
	s_load_dwordx2 s[22:23], s[16:17], 0xe0
	v_lshlrev_b32_e32 v0, 7, v65
	v_lshlrev_b64 v[90:91], 2, v[6:7]
	v_or_b32_e32 v6, 0x700, v66
	s_addc_u32 s37, s19, 0
	v_sub_u32_e32 v165, v164, v0
	v_or_b32_e32 v0, 0x100, v66
	v_lshlrev_b64 v[96:97], 2, v[6:7]
	v_mul_u32_u24_e32 v6, 0x210, v8
	v_lshlrev_b32_e32 v7, 2, v64
	s_add_u32 s38, s18, 0xbc0000
	v_add3_u32 v170, s13, v6, v7
	v_lshlrev_b32_e32 v6, 8, v65
	v_mov_b32_e32 v7, v67
	s_addc_u32 s39, s19, 0
	v_lshlrev_b64 v[106:107], 2, v[0:1]
	v_add_u32_e32 v0, 0, v9
	v_lshlrev_b64 v[72:73], 2, v[66:67]
	v_mul_u32_u24_e32 v10, 12, v65
	v_or_b32_e32 v2, 0x200, v66
	v_mov_b32_e32 v3, v67
	v_or_b32_e32 v4, 0x300, v66
	v_mov_b32_e32 v5, v67
	v_lshl_add_u64 v[102:103], s[28:29], 0, v[6:7]
	s_add_u32 s40, s18, 0xc00000
	v_lshl_add_u64 v[6:7], s[18:19], 0, v[66:67]
	s_mov_b64 s[0:1], 0x70700000
	v_add_u32_e32 v176, 0x18800, v0
	v_mbcnt_lo_u32_b32 v0, -1, 0
	s_mov_b32 s25, 0
	v_cmp_eq_u32_e64 s[6:7], 0, v65
	v_lshl_add_u32 v163, v8, 11, s13
	v_cmp_gt_u32_e64 s[4:5], 16, v65
	v_lshrrev_b32_e32 v166, 2, v65
	v_add_u32_e32 v167, s44, v66
	v_and_b32_e32 v169, 3, v162
	s_waitcnt lgkmcnt(0)
	v_lshl_add_u64 v[74:75], s[8:9], 0, v[72:73]
	v_lshl_add_u64 v[76:77], s[10:11], 0, v[72:73]
	s_movk_i32 s45, 0x100
	s_movk_i32 s46, 0x200
	s_movk_i32 s47, 0x400
	v_lshl_add_u64 v[80:81], s[8:9], 0, v[78:79]
	v_lshl_add_u64 v[82:83], s[10:11], 0, v[78:79]
	v_lshl_add_u64 v[86:87], s[8:9], 0, v[84:85]
	v_lshl_add_u64 v[88:89], s[10:11], 0, v[84:85]
	v_lshl_add_u64 v[92:93], s[8:9], 0, v[90:91]
	v_lshl_add_u64 v[94:95], s[10:11], 0, v[90:91]
	v_lshl_add_u64 v[98:99], s[8:9], 0, v[96:97]
	v_lshl_add_u64 v[100:101], s[10:11], 0, v[96:97]
	v_lshl_add_u32 v171, v65, 4, s13
	s_addc_u32 s41, s19, 0
	s_lshl_b32 s48, s3, 2
	v_lshl_add_u64 v[104:105], v[6:7], 0, s[0:1]
	s_lshl_b32 s49, s20, 4
	s_lshl_b32 s50, s3, 6
	v_lshlrev_b32_e32 v172, 11, v64
	v_add_u32_e32 v173, v165, v10
	v_lshlrev_b64 v[108:109], 2, v[2:3]
	v_lshlrev_b64 v[110:111], 2, v[4:5]
	s_movk_i32 s51, 0x800
	v_mov_b32_e32 v174, 0x3727c5ac
	s_mov_b32 s52, 0xf800000
	v_mov_b32_e32 v175, 0x260
	s_mov_b32 s53, 0x8000
	s_movk_i32 s54, 0x1000
	s_mov_b32 s55, 0x10000
	s_mov_b32 s56, 0x11000
	s_mov_b32 s57, 0x20000
	s_mov_b32 s58, 0x21000
	s_mov_b32 s59, 0x30000
	s_mov_b32 s60, 0x31000
	s_add_i32 s61, 0, 0x27440
	v_lshlrev_b32_e32 v177, 2, v64
	s_movk_i32 s62, 0x4000
	s_mov_b32 s63, 0xff7fc99e
	s_movk_i32 s64, 0x80
	s_movk_i32 s65, 0x2000
	s_mov_b32 s66, 0x40000
	s_mov_b32 s67, 0x80000
	s_mov_b32 s68, 0x100000
	s_mov_b32 s69, 0x200000
	s_mov_b32 s70, 0x400000
	s_mov_b32 s71, 0x800000
	s_mov_b32 s72, 0x1000000
	s_brev_b32 s73, 64
	s_brev_b32 s74, 32
	s_brev_b32 s75, 16
	s_brev_b32 s76, 8
	s_brev_b32 s77, 4
	v_mov_b32_e32 v178, 1
	v_mbcnt_hi_u32_b32 v179, -1, v0
	v_mov_b32_e32 v180, 0xff7fc99e
	s_mov_b32 s78, 0
	s_branch .LBB0_1177

.LBB0_1245:
	s_setprio 0
	s_cmp_gt_i32 s83, 10
	s_cselect_b64 s[0:1], -1, 0
	s_and_b64 s[4:5], s[14:15], s[0:1]
	s_andn2_b64 vcc, exec, s[4:5]
	s_cbranch_vccnz .LBB0_1299
	s_mov_b32 s4, 0
	s_waitcnt vmcnt(0)
	s_waitcnt vmcnt(0) lgkmcnt(0)
	v_mbcnt_lo_u32_b32 v0, -1, s4
	v_mbcnt_hi_u32_b32 v0, -1, v0
	v_or_b32_e32 v0, s92, v0
	v_cmp_eq_u32_e32 vcc, 0, v0
	s_barrier
	s_and_saveexec_b64 s[4:5], vcc
	s_cbranch_execz .LBB0_1298
	s_add_i32 s6, 0, 0x27420
	v_mov_b32_e32 v0, s6
	s_waitcnt vmcnt(0) expcnt(0) lgkmcnt(0)
	ds_read_b32 v2, v0
	s_add_i32 s6, 0, 0x27424
	v_mov_b32_e32 v0, s6
	ds_read_b32 v0, v0
	s_waitcnt lgkmcnt(1)
	v_cmp_ne_u32_e32 vcc, 0, v2
	s_cbranch_vccnz .LBB0_1262
	s_load_dwordx2 s[10:11], s[90:91], 0x4
	s_add_u32 s6, s80, 0x4200
	s_addc_u32 s7, s81, 0
	s_add_u32 s8, s80, 0x4400
	s_addc_u32 s9, s81, 0
	s_waitcnt lgkmcnt(0)
	s_mul_i32 s33, s10, s3
	s_add_u32 s10, s80, 0x4500
	s_mul_i32 s33, s33, s11
	s_addc_u32 s11, s81, 0
	s_add_u32 s12, s80, 0x4600
	s_addc_u32 s13, s81, 0
	s_add_u32 s14, s80, 0x4700
	s_addc_u32 s15, s81, 0
	s_add_u32 s16, s80, 0x4800
	s_addc_u32 s17, s81, 0
	s_add_u32 s18, s80, 0x4900
	s_addc_u32 s19, s81, 0
	s_add_u32 s20, s80, 0x4a00
	s_addc_u32 s21, s81, 0
	s_add_u32 s22, s80, 0x4b00
	s_addc_u32 s23, s81, 0
	s_add_u32 s24, s80, 0x4c00
	s_addc_u32 s25, s81, 0
	s_add_u32 s26, s80, 0x4d00
	s_addc_u32 s27, s81, 0
	s_add_u32 s28, s80, 0x4e00
	s_addc_u32 s29, s81, 0
	s_add_u32 s30, s80, 0x4f00
	s_addc_u32 s31, s81, 0
	s_add_u32 s34, s80, 0x5000
	s_addc_u32 s35, s81, 0
	s_add_u32 s36, s80, 0x5100
	s_addc_u32 s37, s81, 0
	s_add_u32 s38, s80, 0x5200
	s_addc_u32 s39, s81, 0
	s_add_u32 s40, s80, 0x5300
	s_addc_u32 s41, s81, 0
	s_mov_b32 s48, 1
	v_mov_b32_e32 v16, 0
	s_branch .LBB0_1250
